# FFN-in SwiGLU epilogue: the 64 packed v_pk_mul_f32 per unit split into scalar v_mul_f32 pairs (same code size)
# speedup vs baseline: 1.0059x; 1.0059x over previous
.LBB0_228:
	v_mov_b32_e32 v3, v168
	v_mov_b32_e32 v4, v167
	v_exp_f32_e64 v5, -v150
	v_exp_f32_e64 v7, -v151
	s_lshl_b32 s7, s23, 8
	s_lshl_b32 s6, s84, 7
	v_lshlrev_b32_e32 v2, 4, v3
	v_lshlrev_b32_e32 v3, 3, v3
	v_and_or_b32 v2, v2, 16, s6
	s_mov_b32 s6, 0x3e38aa3b
	v_and_b32_e32 v3, -16, v3
	s_add_i32 s7, s7, s77
	v_add3_u32 v6, s7, v4, v3
	v_fma_f32 v4, v5, s6, s6
	v_fma_f32 v5, v7, s6, s6
	v_exp_f32_e64 v7, -v153
	v_exp_f32_e64 v8, -v152
	v_rcp_f32_e32 v4, v4
	v_rcp_f32_e32 v5, v5
	v_fma_f32 v7, v7, s6, s6
	v_fma_f32 v8, v8, s6, s6
	v_rcp_f32_e32 v9, v7
	v_exp_f32_e64 v7, -v146
	v_rcp_f32_e32 v8, v8
	v_mul_f32_e32 v10, v152, v160
	v_mul_f32_e32 v11, v153, v161
	v_mul_f32_e32 v12, v150, v158
	v_mul_f32_e32 v13, v151, v159
	v_fma_f32 v7, v7, s6, s6
	v_mul_f32_e32 v10, v10, v8
	v_mul_f32_e32 v11, v11, v9
	v_mul_f32_e32 v4, v12, v4
	v_mul_f32_e32 v5, v13, v5
	v_exp_f32_e64 v8, -v147
	v_exp_f32_e64 v9, -v148
	v_rcp_f32_e32 v12, v7
	v_exp_f32_e64 v7, -v149
	v_fma_f32 v13, v8, s6, s6
	v_fma_f32 v8, v9, s6, s6
	v_rcp_f32_e32 v8, v8
	v_fma_f32 v7, v7, s6, s6
	v_rcp_f32_e32 v9, v7
	v_mul_f32_e32 v14, v148, v156
	v_mul_f32_e32 v15, v149, v157
	v_rcp_f32_e32 v13, v13
	v_med3_f32 v4, v4, s33, v236
	v_mul_f32_e32 v14, v14, v8
	v_mul_f32_e32 v15, v15, v9
	v_med3_f32 v5, v5, s33, v236
	s_nop 0
	v_cvt_pk_fp8_f32 v8, v4, v5
	v_mul_f32_e32 v16, v146, v154
	v_mul_f32_e32 v17, v147, v155
	v_med3_f32 v7, v10, s33, v236
	v_mul_f32_e32 v4, v16, v12
	v_mul_f32_e32 v5, v17, v13
	v_med3_f32 v9, v11, s33, v236
	v_cvt_pk_fp8_f32 v8, v7, v9 op_sel:[0,0,1]
	v_med3_f32 v4, v4, s33, v236
	v_med3_f32 v5, v5, s33, v236
	s_nop 0
	v_cvt_pk_fp8_f32 v9, v4, v5
	v_med3_f32 v4, v14, s33, v236
	v_med3_f32 v7, v15, s33, v236
	v_exp_f32_e64 v5, -v134
	v_cvt_pk_fp8_f32 v9, v4, v7 op_sel:[0,0,1]
	v_exp_f32_e64 v7, -v135
	v_exp_f32_e64 v10, -v136
	v_fma_f32 v4, v5, s6, s6
	v_rcp_f32_e32 v4, v4
	v_fma_f32 v5, v7, s6, s6
	v_exp_f32_e64 v7, -v137
	v_fma_f32 v10, v10, s6, s6
	v_rcp_f32_e32 v10, v10
	v_rcp_f32_e32 v5, v5
	v_fma_f32 v7, v7, s6, s6
	v_rcp_f32_e32 v11, v7
	v_exp_f32_e64 v7, -v130
	v_mul_f32_e32 v12, v136, v144
	v_mul_f32_e32 v13, v137, v145
	v_mul_f32_e32 v14, v134, v142
	v_mul_f32_e32 v15, v135, v143
	v_mul_f32_e32 v10, v12, v10
	v_mul_f32_e32 v11, v13, v11
	v_fma_f32 v7, v7, s6, s6
	v_exp_f32_e64 v13, -v131
	v_mul_f32_e32 v4, v14, v4
	v_mul_f32_e32 v5, v15, v5
	v_exp_f32_e64 v14, -v132
	v_rcp_f32_e32 v12, v7
	v_exp_f32_e64 v7, -v133
	v_fma_f32 v13, v13, s6, s6
	v_fma_f32 v14, v14, s6, s6
	v_rcp_f32_e32 v13, v13
	v_fma_f32 v7, v7, s6, s6
	v_rcp_f32_e32 v14, v14
	v_rcp_f32_e32 v15, v7
	v_mul_f32_e32 v18, v130, v138
	v_mul_f32_e32 v19, v131, v139
	v_mul_f32_e32 v16, v132, v140
	v_mul_f32_e32 v17, v133, v141
	v_mul_f32_e32 v12, v18, v12
	v_mul_f32_e32 v13, v19, v13
	v_med3_f32 v4, v4, s33, v236
	v_med3_f32 v5, v5, s33, v236
	v_med3_f32 v7, v10, s33, v236
	s_nop 0
	v_mul_f32_e32 v14, v16, v14
	v_mul_f32_e32 v15, v17, v15
	v_med3_f32 v16, v11, s33, v236
	v_cvt_pk_fp8_f32 v10, v4, v5
	v_med3_f32 v4, v12, s33, v236
	v_med3_f32 v5, v13, s33, v236
	s_nop 0
	v_cvt_pk_fp8_f32 v11, v4, v5
	v_med3_f32 v4, v14, s33, v236
	v_med3_f32 v5, v15, s33, v236
	v_cvt_pk_fp8_f32 v10, v7, v16 op_sel:[0,0,1]
	v_cvt_pk_fp8_f32 v11, v4, v5 op_sel:[0,0,1]
	v_exp_f32_e64 v7, -v118
	v_or_b32_e32 v2, s78, v2
	v_mov_b64_e32 v[4:5], s[34:35]
	s_movk_i32 s7, 0x1600
	v_ashrrev_i32_e32 v3, 31, v2
	v_mad_i64_i32 v[12:13], s[14:15], v6, s7, v[4:5]
	v_permlane32_swap_b32_e32 v8, v10
	v_permlane32_swap_b32_e32 v9, v11
	v_lshl_add_u64 v[12:13], v[12:13], 0, v[2:3]
	v_fma_f32 v7, v7, s6, s6
	global_store_dwordx4 v[12:13], v[8:11], off
	v_mul_f32_e32 v12, v120, v128
	v_mul_f32_e32 v13, v121, v129
	v_mul_f32_e32 v14, v118, v126
	v_mul_f32_e32 v15, v119, v127
	v_rcp_f32_e32 v8, v7
	v_exp_f32_e64 v7, -v120
	v_exp_f32_e64 v11, -v121
	v_exp_f32_e64 v9, -v119
	v_mul_f32_e32 v18, v114, v122
	v_mul_f32_e32 v19, v115, v123
	v_fma_f32 v7, v7, s6, s6
	v_rcp_f32_e32 v10, v7
	v_fma_f32 v7, v11, s6, s6
	v_rcp_f32_e32 v11, v7
	v_exp_f32_e64 v7, -v114
	v_fma_f32 v9, v9, s6, s6
	v_rcp_f32_e32 v9, v9
	v_mul_f32_e32 v10, v12, v10
	v_mul_f32_e32 v11, v13, v11
	v_fma_f32 v7, v7, s6, s6
	v_exp_f32_e64 v13, -v115
	v_rcp_f32_e32 v12, v7
	v_exp_f32_e64 v7, -v117
	v_mul_f32_e32 v8, v14, v8
	v_mul_f32_e32 v9, v15, v9
	v_exp_f32_e64 v14, -v116
	v_fma_f32 v13, v13, s6, s6
	v_fma_f32 v7, v7, s6, s6
	v_rcp_f32_e32 v15, v7
	v_rcp_f32_e32 v13, v13
	v_med3_f32 v7, v8, s33, v236
	v_med3_f32 v9, v9, s33, v236
	s_nop 0
	v_cvt_pk_fp8_f32 v8, v7, v9
	v_fma_f32 v14, v14, s6, s6
	v_rcp_f32_e32 v14, v14
	v_mul_f32_e32 v12, v18, v12
	v_mul_f32_e32 v13, v19, v13
	v_med3_f32 v7, v10, s33, v236
	v_med3_f32 v9, v11, s33, v236
	v_cvt_pk_fp8_f32 v8, v7, v9 op_sel:[0,0,1]
	v_med3_f32 v7, v12, s33, v236
	v_med3_f32 v10, v13, s33, v236
	s_nop 0
	v_cvt_pk_fp8_f32 v9, v7, v10
	v_mul_f32_e32 v16, v116, v124
	v_mul_f32_e32 v17, v117, v125
	v_exp_f32_e64 v12, -v100
	v_mul_f32_e32 v14, v16, v14
	v_mul_f32_e32 v15, v17, v15
	v_exp_f32_e64 v13, -v101
	v_med3_f32 v7, v14, s33, v236
	v_med3_f32 v11, v15, s33, v236
	v_cvt_pk_fp8_f32 v9, v7, v11 op_sel:[0,0,1]
	v_exp_f32_e64 v7, -v99
	v_exp_f32_e64 v10, -v98
	v_mul_f32_e32 v14, v100, v112
	v_mul_f32_e32 v15, v101, v113
	v_mul_f32_e32 v16, v98, v110
	v_mul_f32_e32 v17, v99, v111
	v_fma_f32 v7, v7, s6, s6
	v_rcp_f32_e32 v11, v7
	v_fma_f32 v7, v12, s6, s6
	v_rcp_f32_e32 v12, v7
	v_fma_f32 v7, v13, s6, s6
	v_rcp_f32_e32 v13, v7
	v_fma_f32 v10, v10, s6, s6
	v_exp_f32_e64 v7, -v90
	v_rcp_f32_e32 v10, v10
	v_mul_f32_e32 v12, v14, v12
	v_mul_f32_e32 v13, v15, v13
	v_exp_f32_e64 v15, -v91
	v_fma_f32 v7, v7, s6, s6
	v_mul_f32_e32 v10, v16, v10
	v_mul_f32_e32 v11, v17, v11
	v_exp_f32_e64 v16, -v92
	v_rcp_f32_e32 v14, v7
	v_exp_f32_e64 v7, -v93
	v_fma_f32 v15, v15, s6, s6
	v_rcp_f32_e32 v15, v15
	v_fma_f32 v16, v16, s6, s6
	v_fma_f32 v7, v7, s6, s6
	v_mul_f32_e32 v20, v90, v106
	v_mul_f32_e32 v21, v91, v107
	v_rcp_f32_e32 v16, v16
	v_rcp_f32_e32 v17, v7
	v_mul_f32_e32 v14, v20, v14
	v_mul_f32_e32 v15, v21, v15
	v_med3_f32 v7, v10, s33, v236
	v_med3_f32 v11, v11, s33, v236
	s_nop 0
	v_cvt_pk_fp8_f32 v10, v7, v11
	v_med3_f32 v7, v14, s33, v236
	v_med3_f32 v14, v15, s33, v236
	s_nop 0
	v_cvt_pk_fp8_f32 v11, v7, v14
	v_mul_f32_e32 v18, v92, v108
	v_mul_f32_e32 v19, v93, v109
	v_med3_f32 v12, v12, s33, v236
	v_mul_f32_e32 v16, v18, v16
	v_mul_f32_e32 v17, v19, v17
	v_med3_f32 v13, v13, s33, v236
	v_cvt_pk_fp8_f32 v10, v12, v13 op_sel:[0,0,1]
	v_med3_f32 v7, v16, s33, v236
	v_med3_f32 v12, v17, s33, v236
	v_cvt_pk_fp8_f32 v11, v7, v12 op_sel:[0,0,1]
	v_add_u32_e32 v7, 32, v6
	v_mad_i64_i32 v[12:13], s[14:15], v7, s7, v[4:5]
	v_exp_f32_e64 v7, -v86
	v_permlane32_swap_b32_e32 v8, v10
	v_permlane32_swap_b32_e32 v9, v11
	v_lshl_add_u64 v[12:13], v[12:13], 0, v[2:3]
	v_fma_f32 v7, v7, s6, s6
	global_store_dwordx4 v[12:13], v[8:11], off
	v_mul_f32_e32 v12, v88, v104
	v_mul_f32_e32 v13, v89, v105
	v_mul_f32_e32 v14, v86, v102
	v_mul_f32_e32 v15, v87, v103
	v_rcp_f32_e32 v8, v7
	v_exp_f32_e64 v7, -v88
	v_exp_f32_e64 v11, -v89
	v_exp_f32_e64 v9, -v87
	v_mul_f32_e32 v18, v82, v94
	v_mul_f32_e32 v19, v83, v95
	v_fma_f32 v7, v7, s6, s6
	v_rcp_f32_e32 v10, v7
	v_fma_f32 v7, v11, s6, s6
	v_rcp_f32_e32 v11, v7
	v_exp_f32_e64 v7, -v82
	v_fma_f32 v9, v9, s6, s6
	v_rcp_f32_e32 v9, v9
	v_mul_f32_e32 v10, v12, v10
	v_mul_f32_e32 v11, v13, v11
	v_fma_f32 v7, v7, s6, s6
	v_exp_f32_e64 v13, -v83
	v_rcp_f32_e32 v12, v7
	v_exp_f32_e64 v7, -v85
	v_mul_f32_e32 v8, v14, v8
	v_mul_f32_e32 v9, v15, v9
	v_exp_f32_e64 v14, -v84
	v_fma_f32 v13, v13, s6, s6
	v_fma_f32 v7, v7, s6, s6
	v_rcp_f32_e32 v15, v7
	v_rcp_f32_e32 v13, v13
	v_med3_f32 v7, v8, s33, v236
	v_med3_f32 v9, v9, s33, v236
	s_nop 0
	v_cvt_pk_fp8_f32 v8, v7, v9
	v_fma_f32 v14, v14, s6, s6
	v_rcp_f32_e32 v14, v14
	v_mul_f32_e32 v12, v18, v12
	v_mul_f32_e32 v13, v19, v13
	v_med3_f32 v7, v10, s33, v236
	v_med3_f32 v9, v11, s33, v236
	v_cvt_pk_fp8_f32 v8, v7, v9 op_sel:[0,0,1]
	v_med3_f32 v7, v12, s33, v236
	v_med3_f32 v10, v13, s33, v236
	s_nop 0
	v_cvt_pk_fp8_f32 v9, v7, v10
	v_mul_f32_e32 v16, v84, v96
	v_mul_f32_e32 v17, v85, v97
	v_exp_f32_e64 v12, -v72
	v_mul_f32_e32 v14, v16, v14
	v_mul_f32_e32 v15, v17, v15
	v_exp_f32_e64 v13, -v73
	v_med3_f32 v7, v14, s33, v236
	v_med3_f32 v11, v15, s33, v236
	v_cvt_pk_fp8_f32 v9, v7, v11 op_sel:[0,0,1]
	v_exp_f32_e64 v7, -v71
	v_exp_f32_e64 v10, -v70
	v_mul_f32_e32 v14, v72, v80
	v_mul_f32_e32 v15, v73, v81
	v_mul_f32_e32 v16, v70, v78
	v_mul_f32_e32 v17, v71, v79
	v_fma_f32 v7, v7, s6, s6
	v_rcp_f32_e32 v11, v7
	v_fma_f32 v7, v12, s6, s6
	v_rcp_f32_e32 v12, v7
	v_fma_f32 v7, v13, s6, s6
	v_rcp_f32_e32 v13, v7
	v_fma_f32 v10, v10, s6, s6
	v_exp_f32_e64 v7, -v66
	v_rcp_f32_e32 v10, v10
	v_mul_f32_e32 v12, v14, v12
	v_mul_f32_e32 v13, v15, v13
	v_exp_f32_e64 v15, -v67
	v_fma_f32 v7, v7, s6, s6
	v_mul_f32_e32 v10, v16, v10
	v_mul_f32_e32 v11, v17, v11
	v_exp_f32_e64 v16, -v68
	v_rcp_f32_e32 v14, v7
	v_exp_f32_e64 v7, -v69
	v_fma_f32 v15, v15, s6, s6
	v_rcp_f32_e32 v15, v15
	v_fma_f32 v16, v16, s6, s6
	v_fma_f32 v7, v7, s6, s6
	v_mul_f32_e32 v20, v66, v74
	v_mul_f32_e32 v21, v67, v75
	v_rcp_f32_e32 v16, v16
	v_rcp_f32_e32 v17, v7
	v_mul_f32_e32 v14, v20, v14
	v_mul_f32_e32 v15, v21, v15
	v_med3_f32 v7, v10, s33, v236
	v_med3_f32 v11, v11, s33, v236
	s_nop 0
	v_cvt_pk_fp8_f32 v10, v7, v11
	v_med3_f32 v7, v14, s33, v236
	v_med3_f32 v14, v15, s33, v236
	s_nop 0
	v_cvt_pk_fp8_f32 v11, v7, v14
	v_mul_f32_e32 v18, v68, v76
	v_mul_f32_e32 v19, v69, v77
	v_med3_f32 v12, v12, s33, v236
	v_mul_f32_e32 v16, v18, v16
	v_mul_f32_e32 v17, v19, v17
	v_med3_f32 v13, v13, s33, v236
	v_cvt_pk_fp8_f32 v10, v12, v13 op_sel:[0,0,1]
	v_med3_f32 v7, v16, s33, v236
	v_med3_f32 v12, v17, s33, v236
	v_cvt_pk_fp8_f32 v11, v7, v12 op_sel:[0,0,1]
	v_exp_f32_e64 v7, -v58
	v_add_u32_e32 v22, 0x80, v6
	v_mad_i64_i32 v[12:13], s[14:15], v22, s7, v[4:5]
	v_permlane32_swap_b32_e32 v8, v10
	v_permlane32_swap_b32_e32 v9, v11
	v_lshl_add_u64 v[12:13], v[12:13], 0, v[2:3]
	v_fma_f32 v7, v7, s6, s6
	global_store_dwordx4 v[12:13], v[8:11], off
	v_mul_f32_e32 v12, v60, v64
	v_mul_f32_e32 v13, v61, v65
	v_mul_f32_e32 v14, v58, v62
	v_mul_f32_e32 v15, v59, v63
	v_rcp_f32_e32 v8, v7
	v_exp_f32_e64 v7, -v60
	v_exp_f32_e64 v11, -v61
	v_exp_f32_e64 v9, -v59
	v_mul_f32_e32 v18, v50, v54
	v_mul_f32_e32 v19, v51, v55
	v_fma_f32 v7, v7, s6, s6
	v_rcp_f32_e32 v10, v7
	v_fma_f32 v7, v11, s6, s6
	v_rcp_f32_e32 v11, v7
	v_exp_f32_e64 v7, -v50
	v_fma_f32 v9, v9, s6, s6
	v_rcp_f32_e32 v9, v9
	v_mul_f32_e32 v10, v12, v10
	v_mul_f32_e32 v11, v13, v11
	v_fma_f32 v7, v7, s6, s6
	v_exp_f32_e64 v13, -v51
	v_rcp_f32_e32 v12, v7
	v_exp_f32_e64 v7, -v53
	v_mul_f32_e32 v8, v14, v8
	v_mul_f32_e32 v9, v15, v9
	v_exp_f32_e64 v14, -v52
	v_fma_f32 v13, v13, s6, s6
	v_fma_f32 v7, v7, s6, s6
	v_rcp_f32_e32 v15, v7
	v_rcp_f32_e32 v13, v13
	v_med3_f32 v7, v8, s33, v236
	v_med3_f32 v9, v9, s33, v236
	s_nop 0
	v_cvt_pk_fp8_f32 v8, v7, v9
	v_fma_f32 v14, v14, s6, s6
	v_rcp_f32_e32 v14, v14
	v_mul_f32_e32 v12, v18, v12
	v_mul_f32_e32 v13, v19, v13
	v_med3_f32 v7, v10, s33, v236
	v_med3_f32 v9, v11, s33, v236
	v_cvt_pk_fp8_f32 v8, v7, v9 op_sel:[0,0,1]
	v_med3_f32 v7, v12, s33, v236
	v_med3_f32 v10, v13, s33, v236
	s_nop 0
	v_cvt_pk_fp8_f32 v9, v7, v10
	v_mul_f32_e32 v16, v52, v56
	v_mul_f32_e32 v17, v53, v57
	v_exp_f32_e64 v12, -v44
	v_mul_f32_e32 v14, v16, v14
	v_mul_f32_e32 v15, v17, v15
	v_exp_f32_e64 v13, -v45
	v_med3_f32 v7, v14, s33, v236
	v_med3_f32 v11, v15, s33, v236
	v_cvt_pk_fp8_f32 v9, v7, v11 op_sel:[0,0,1]
	v_exp_f32_e64 v7, -v43
	v_exp_f32_e64 v10, -v42
	v_mul_f32_e32 v14, v44, v48
	v_mul_f32_e32 v15, v45, v49
	v_mul_f32_e32 v16, v42, v46
	v_mul_f32_e32 v17, v43, v47
	v_fma_f32 v7, v7, s6, s6
	v_rcp_f32_e32 v11, v7
	v_fma_f32 v7, v12, s6, s6
	v_rcp_f32_e32 v12, v7
	v_fma_f32 v7, v13, s6, s6
	v_rcp_f32_e32 v13, v7
	v_fma_f32 v10, v10, s6, s6
	v_exp_f32_e64 v7, -v34
	v_rcp_f32_e32 v10, v10
	v_mul_f32_e32 v12, v14, v12
	v_mul_f32_e32 v13, v15, v13
	v_exp_f32_e64 v15, -v35
	v_fma_f32 v7, v7, s6, s6
	v_mul_f32_e32 v10, v16, v10
	v_mul_f32_e32 v11, v17, v11
	v_exp_f32_e64 v16, -v36
	v_rcp_f32_e32 v14, v7
	v_exp_f32_e64 v7, -v37
	v_fma_f32 v15, v15, s6, s6
	v_rcp_f32_e32 v15, v15
	v_fma_f32 v16, v16, s6, s6
	v_fma_f32 v7, v7, s6, s6
	v_mul_f32_e32 v20, v34, v38
	v_mul_f32_e32 v21, v35, v39
	v_rcp_f32_e32 v16, v16
	v_rcp_f32_e32 v17, v7
	v_mul_f32_e32 v14, v20, v14
	v_mul_f32_e32 v15, v21, v15
	v_med3_f32 v7, v10, s33, v236
	v_med3_f32 v11, v11, s33, v236
	s_nop 0
	v_cvt_pk_fp8_f32 v10, v7, v11
	v_med3_f32 v7, v14, s33, v236
	v_med3_f32 v14, v15, s33, v236
	s_nop 0
	v_cvt_pk_fp8_f32 v11, v7, v14
	v_mul_f32_e32 v18, v36, v40
	v_mul_f32_e32 v19, v37, v41
	v_med3_f32 v12, v12, s33, v236
	v_mul_f32_e32 v16, v18, v16
	v_mul_f32_e32 v17, v19, v17
	v_med3_f32 v13, v13, s33, v236
	v_cvt_pk_fp8_f32 v10, v12, v13 op_sel:[0,0,1]
	v_med3_f32 v7, v16, s33, v236
	v_med3_f32 v12, v17, s33, v236
	v_cvt_pk_fp8_f32 v11, v7, v12 op_sel:[0,0,1]
	v_add_u32_e32 v6, 0xa0, v6
	v_mad_i64_i32 v[4:5], s[6:7], v6, s7, v[4:5]
	s_mov_b32 s62, 0x41200000
	v_permlane32_swap_b32_e32 v8, v10
	v_permlane32_swap_b32_e32 v9, v11
	v_lshl_add_u64 v[2:3], v[4:5], 0, v[2:3]
	s_andn2_b64 vcc, exec, s[38:39]
	s_mov_b64 s[6:7], -1
	s_mov_b32 s63, 0x41300000
	global_store_dwordx4 v[2:3], v[8:11], off
	s_cbranch_vccnz .LBB0_221
	s_andn2_b64 vcc, exec, s[2:3]
	s_cbranch_vccnz .LBB0_220
	s_barrier
	s_branch .LBB0_220
